# diff-attention unit prologue: K(0)/V(0) LDS-DMAs issued right behind the Q loads instead of after the Q wait ladder (Q and K/V latencies overlap)
# speedup vs baseline: 1.0030x; 1.0030x over previous
.LBB0_564:
	s_xor_b64 s[12:13], s[14:15], -1
	s_and_b64 s[14:15], s[14:15], exec
	s_cselect_b32 s39, s31, s34
	s_mul_i32 s14, s39, 0x1a00
	v_mov_b32_e32 v128, v231
	s_add_u32 s16, s6, s14
	s_addc_u32 s17, s7, 0
	v_readfirstlane_b32 s18, v128
	v_lshlrev_b32_e32 v0, 3, v128
	s_ashr_i32 s14, s18, 6
	v_and_b32_e32 v129, 0x78, v0
	v_bfe_u32 v130, v128, 4, 2
	s_lshl_b32 s38, s14, 5
	v_lshlrev_b32_e32 v208, 1, v129
	v_or_b32_e32 v2, 4, v130
	v_or_b32_e32 v8, 8, v130
	v_or_b32_e32 v10, 12, v130
	v_lshl_add_u64 v[28:29], s[16:17], 0, v[208:209]
	v_or_b32_e32 v32, s38, v130
	v_or_b32_e32 v33, s38, v2
	v_or_b32_e32 v34, s38, v8
	v_or_b32_e32 v35, s38, v10
	v_mad_i64_i32 v[0:1], s[16:17], v32, s62, v[28:29]
	v_mad_i64_i32 v[4:5], s[16:17], v33, s62, v[28:29]
	v_mad_i64_i32 v[8:9], s[16:17], v34, s62, v[28:29]
	v_mad_i64_i32 v[12:13], s[16:17], v35, s62, v[28:29]
	global_load_dwordx4 v[0:3], v[0:1], off
	s_nop 0
	global_load_dwordx4 v[4:7], v[4:5], off
	s_nop 0
	global_load_dwordx4 v[8:11], v[8:9], off
	s_nop 0
	global_load_dwordx4 v[12:15], v[12:13], off
	v_or_b32_e32 v36, 16, v32
	v_mad_i64_i32 v[16:17], s[16:17], v36, s62, v[28:29]
	global_load_dwordx4 v[16:19], v[16:17], off
	v_or_b32_e32 v20, 20, v130
	v_or_b32_e32 v37, s38, v20
	v_mad_i64_i32 v[20:21], s[16:17], v37, s62, v[28:29]
	global_load_dwordx4 v[20:23], v[20:21], off
	v_or_b32_e32 v24, 24, v130
	v_or_b32_e32 v38, s38, v24
	v_mad_i64_i32 v[24:25], s[16:17], v38, s62, v[28:29]
	v_or_b32_e32 v30, 28, v130
	global_load_dwordx4 v[24:27], v[24:25], off
	v_or_b32_e32 v39, s38, v30
	v_mad_i64_i32 v[28:29], s[16:17], v39, s62, v[28:29]
	global_load_dwordx4 v[28:31], v[28:29], off
	s_lshl_b32 s16, s14, 3
	v_bitop3_b32 v56, s16, v128, v130 bitop3:0x36
	v_or_b32_e32 v55, s16, v130
	v_lshlrev_b32_e32 v56, 3, v56
	v_mul_lo_u32 v57, v55, s96
	v_and_b32_e32 v133, 0x78, v56
	v_bitop3_b32 v55, v55, v128, 4 bitop3:0x36
	v_lshlrev_b32_e32 v132, 5, v130
	v_or_b32_e32 v56, v133, v57
	v_lshlrev_b32_e32 v55, 3, v55
	v_lshlrev_b32_e32 v208, 1, v56
	v_bitop3_b32 v56, v57, v132, v129 bitop3:0xf6
	v_add_u32_e32 v57, 0x3400, v57
	v_and_b32_e32 v134, 0x78, v55
	v_or_b32_e32 v55, v134, v57
	s_lshl_b32 s16, s14, 11
	v_lshlrev_b32_e32 v56, 1, v56
	v_lshlrev_b32_e32 v58, 1, v55
	v_bitop3_b32 v55, v57, v132, v129 bitop3:0xf6
	v_lshl_add_u64 v[62:63], s[6:7], 0, v[208:209]
	s_add_i32 s44, s16, 0
	v_mov_b32_e32 v57, v209
	v_lshl_add_u64 v[62:63], v[62:63], 0, s[86:87]
	s_mov_b32 m0, s44
	v_lshl_add_u64 v[56:57], s[6:7], 0, v[56:57]
	global_load_lds_dwordx4 v[62:63], off
	v_lshl_add_u64 v[56:57], v[56:57], 0, s[88:89]
	s_add_i32 m0, s44, 0x8000
	v_mov_b32_e32 v59, v209
	global_load_lds_dwordx4 v[56:57], off
	v_lshl_add_u64 v[56:57], s[6:7], 0, v[58:59]
	v_lshlrev_b32_e32 v60, 1, v55
	v_lshl_add_u64 v[56:57], v[56:57], 0, s[86:87]
	s_add_i32 m0, s44, 0x400
	v_mov_b32_e32 v61, v209
	global_load_lds_dwordx4 v[56:57], off
	v_lshl_add_u64 v[56:57], s[6:7], 0, v[60:61]
	v_lshl_add_u64 v[56:57], v[56:57], 0, s[88:89]
	s_add_i32 m0, s44, 0x8400
	s_nop 0
	global_load_lds_dwordx4 v[56:57], off
	v_xor_b32_e32 v40, v130, v128
	v_bitop3_b32 v41, v130, v128, 4 bitop3:0x36
	v_bitop3_b32 v42, v130, v128, 8 bitop3:0x36
	v_bitop3_b32 v43, v130, v128, 12 bitop3:0x36
	v_lshlrev_b32_e32 v40, 4, v40
	v_lshlrev_b32_e32 v41, 4, v41
	v_lshlrev_b32_e32 v42, 4, v42
	v_lshlrev_b32_e32 v43, 4, v43
	v_and_b32_e32 v40, 0xf0, v40
	v_lshlrev_b32_e32 v32, 8, v32
	v_and_b32_e32 v41, 0xf0, v41
	v_and_b32_e32 v42, 0xf0, v42
	v_and_b32_e32 v43, 0xf0, v43
	v_lshlrev_b32_e32 v33, 8, v33
	v_lshlrev_b32_e32 v34, 8, v34
	v_lshlrev_b32_e32 v35, 8, v35
	v_add3_u32 v32, s65, v32, v40
	s_and_b32 s16, s18, 0x3fffffc0
	v_add3_u32 v33, s65, v33, v41
	v_add3_u32 v34, s65, v34, v42
	v_add3_u32 v35, s65, v35, v43
	v_lshlrev_b32_e32 v36, 8, v36
	s_lshl_b32 s16, s16, 2
	s_add_i32 s40, s16, 0
	s_lshl_b32 s16, s14, 3
	v_bitop3_b32 v56, s16, v128, v130 bitop3:0x36
	v_or_b32_e32 v55, s16, v130
	v_lshlrev_b32_e32 v56, 3, v56
	v_mul_lo_u32 v57, v55, s96
	v_and_b32_e32 v133, 0x78, v56
	v_bitop3_b32 v55, v55, v128, 4 bitop3:0x36
	v_lshlrev_b32_e32 v132, 5, v130
	v_or_b32_e32 v56, v133, v57
	v_lshlrev_b32_e32 v55, 3, v55
	v_lshlrev_b32_e32 v208, 1, v56
	v_bitop3_b32 v56, v57, v132, v129 bitop3:0xf6
	v_add_u32_e32 v57, 0x3400, v57
	s_waitcnt vmcnt(11)
	ds_write_b128 v32, v[0:3]
	s_waitcnt vmcnt(10)
	ds_write_b128 v33, v[4:7]
	s_waitcnt vmcnt(9)
	ds_write_b128 v34, v[8:11]
	s_waitcnt vmcnt(8)
	ds_write_b128 v35, v[12:15]
	v_bitop3_b32 v1, v130, v128, 20 bitop3:0x36
	v_add3_u32 v0, s65, v36, v40
	v_lshlrev_b32_e32 v1, 4, v1
	s_waitcnt vmcnt(7)
	ds_write_b128 v0, v[16:19]
	v_lshlrev_b32_e32 v0, 8, v37
	v_and_b32_e32 v1, 0xf0, v1
	v_add3_u32 v0, s65, v0, v1
	v_bitop3_b32 v1, v130, v128, 24 bitop3:0x36
	v_lshlrev_b32_e32 v1, 4, v1
	s_waitcnt vmcnt(6)
	ds_write_b128 v0, v[20:23]
	v_lshlrev_b32_e32 v0, 8, v38
	v_and_b32_e32 v1, 0xf0, v1
	v_add3_u32 v0, s65, v0, v1
	v_bitop3_b32 v1, v130, v128, 28 bitop3:0x36
	v_lshlrev_b32_e32 v1, 4, v1
	v_and_b32_e32 v134, 0x78, v55
	s_waitcnt vmcnt(5)
	ds_write_b128 v0, v[24:27]
	v_lshlrev_b32_e32 v0, 8, v39
	v_and_b32_e32 v1, 0xf0, v1
	v_or_b32_e32 v55, v134, v57
	s_lshl_b32 s16, s14, 11
	v_add3_u32 v0, s65, v0, v1
	v_lshlrev_b32_e32 v56, 1, v56
	v_lshlrev_b32_e32 v58, 1, v55
	v_bitop3_b32 v55, v57, v132, v129 bitop3:0xf6
	v_lshl_add_u64 v[62:63], s[6:7], 0, v[208:209]
	s_add_i32 s44, s16, 0
	v_mov_b32_e32 v57, v209
	s_waitcnt vmcnt(4)
	ds_write_b128 v0, v[28:31]
	v_mov_b32_e32 v64, v209
	v_mov_b32_e32 v32, v209
	v_mov_b32_e32 v16, v209
	v_mov_b32_e32 v0, v209
	v_mov_b32_e32 v112, v209
	v_mov_b32_e32 v96, v209
	v_mov_b32_e32 v80, v209
	v_mov_b32_e32 v48, v209
	v_lshl_add_u64 v[62:63], v[62:63], 0, s[86:87]
	s_mov_b32 m0, s44
	v_lshl_add_u64 v[56:57], s[6:7], 0, v[56:57]
	v_lshl_add_u64 v[56:57], v[56:57], 0, s[88:89]
	s_add_i32 m0, s44, 0x8000
	v_mov_b32_e32 v59, v209
	v_lshl_add_u64 v[56:57], s[6:7], 0, v[58:59]
	v_lshlrev_b32_e32 v60, 1, v55
	v_lshl_add_u64 v[56:57], v[56:57], 0, s[86:87]
	s_add_i32 m0, s44, 0x400
	v_mov_b32_e32 v61, v209
	v_lshl_add_u64 v[56:57], s[6:7], 0, v[60:61]
	v_lshl_add_u64 v[56:57], v[56:57], 0, s[88:89]
	s_add_i32 m0, s44, 0x8400
	v_bfe_u32 v135, v128, 5, 1
	v_and_b32_e32 v235, 63, v128
	v_and_b32_e32 v131, 31, v128
	v_and_b32_e32 v136, 15, v128
	v_bfe_u32 v137, v128, 2, 2
	v_and_b32_e32 v139, 16, v128
	v_lshlrev_b32_e32 v140, 2, v128
	v_bitop3_b32 v128, v135, v128, 15 bitop3:0x78
	v_lshlrev_b32_e32 v240, 4, v128
	v_bitop3_b32 v128, v135, v136, 2 bitop3:0x36
	v_lshlrev_b32_e32 v241, 4, v128
	v_bitop3_b32 v128, v135, v136, 4 bitop3:0x36
	v_lshlrev_b32_e32 v242, 4, v128
	v_bitop3_b32 v128, v135, v136, 6 bitop3:0x36
	v_lshlrev_b32_e32 v243, 4, v128
	v_bitop3_b32 v128, v135, v136, 8 bitop3:0x36
	v_lshlrev_b32_e32 v244, 4, v128
	v_bitop3_b32 v128, v135, v136, 10 bitop3:0x36
	v_lshlrev_b32_e32 v245, 4, v128
	v_bitop3_b32 v128, v135, v136, 12 bitop3:0x36
	s_add_i32 s16, s38, s39
	v_lshlrev_b32_e32 v246, 4, v128
	v_bitop3_b32 v128, v135, v136, 14 bitop3:0x36
	v_or_b32_e32 v44, s38, v131
	s_add_i32 s40, s40, 0x10000
	v_lshl_add_u32 v237, v131, 8, 0
	v_lshlrev_b32_e32 v247, 4, v128
	v_lshlrev_b32_e32 v128, 4, v135
	v_add_lshl_u32 v131, s16, v131, 2
	v_add_u32_e32 v249, s40, v128
	v_sub_u32_e32 v128, v128, v131
	s_mulk_i32 s14, 0x6800
	v_add_u32_e32 v250, s97, v128
	v_mov_b32_e32 v128, s14
	v_mad_u32_u24 v128, v130, s96, v128
	v_or_b32_e32 v131, v128, v133
	s_addk_i32 s14, 0x3400
	v_lshlrev_b32_e32 v208, 1, v131
	v_mov_b32_e32 v131, s14
	v_mad_u32_u24 v130, v130, s96, v131
	v_or_b32_e32 v130, v130, v134
	s_ashr_i32 s17, s16, 31
	v_lshl_add_u64 v[210:211], s[8:9], 0, v[208:209]
	v_lshlrev_b32_e32 v208, 1, v130
	v_bitop3_b32 v128, v132, v128, v129 bitop3:0xde
	s_lshr_b32 s15, s39, 6
	s_lshr_b32 s17, s17, 26
	v_lshlrev_b32_e32 v138, 8, v137
	v_and_or_b32 v139, v140, 12, v139
	v_lshl_add_u64 v[216:217], s[8:9], 0, v[208:209]
	v_lshlrev_b32_e32 v208, 1, v128
	s_add_i32 s42, s15, 4
	s_add_i32 s17, s16, s17
	v_lshl_or_b32 v138, v135, 10, v138
	v_lshlrev_b32_e32 v139, 1, v139
	s_mul_i32 s15, s15, 0x68000
	v_lshl_add_u64 v[218:219], s[10:11], 0, v[208:209]
	v_add_u32_e32 v208, 0x6800, v208
	s_mov_b32 s41, 1
	v_lshl_add_u32 v236, v44, 8, s65
	s_mov_b32 s43, 0
	v_mov_b32_e32 v65, v64
	v_mov_b32_e32 v66, v64
	v_mov_b32_e32 v67, v64
	v_mov_b32_e32 v68, v64
	v_mov_b32_e32 v69, v64
	v_mov_b32_e32 v70, v64
	v_mov_b32_e32 v71, v64
	v_mov_b32_e32 v72, v64
	v_mov_b32_e32 v73, v64
	v_mov_b32_e32 v74, v64
	v_mov_b32_e32 v75, v64
	v_mov_b32_e32 v76, v64
	v_mov_b32_e32 v77, v64
	v_mov_b32_e32 v78, v64
	v_mov_b32_e32 v79, v64
	v_mov_b32_e32 v33, v32
	v_mov_b32_e32 v34, v32
	v_mov_b32_e32 v35, v32
	v_mov_b32_e32 v36, v32
	v_mov_b32_e32 v37, v32
	v_mov_b32_e32 v38, v32
	v_mov_b32_e32 v39, v32
	v_mov_b32_e32 v40, v32
	v_mov_b32_e32 v41, v32
	v_mov_b32_e32 v42, v32
	v_mov_b32_e32 v43, v32
	v_mov_b32_e32 v44, v32
	v_mov_b32_e32 v45, v32
	v_mov_b32_e32 v46, v32
	v_mov_b32_e32 v47, v32
	v_mov_b32_e32 v17, v16
	v_mov_b32_e32 v18, v16
	v_mov_b32_e32 v19, v16
	v_mov_b32_e32 v20, v16
	v_mov_b32_e32 v21, v16
	v_mov_b32_e32 v22, v16
	v_mov_b32_e32 v23, v16
	v_mov_b32_e32 v24, v16
	v_mov_b32_e32 v25, v16
	v_mov_b32_e32 v26, v16
	v_mov_b32_e32 v27, v16
	v_mov_b32_e32 v28, v16
	v_mov_b32_e32 v29, v16
	v_mov_b32_e32 v30, v16
	v_mov_b32_e32 v31, v16
	v_mov_b32_e32 v1, v0
	v_mov_b32_e32 v2, v0
	v_mov_b32_e32 v3, v0
	v_mov_b32_e32 v4, v0
	v_mov_b32_e32 v5, v0
	v_mov_b32_e32 v6, v0
	v_mov_b32_e32 v7, v0
	v_mov_b32_e32 v8, v0
	v_mov_b32_e32 v9, v0
	v_mov_b32_e32 v10, v0
	v_mov_b32_e32 v11, v0
	v_mov_b32_e32 v12, v0
	v_mov_b32_e32 v13, v0
	v_mov_b32_e32 v14, v0
	v_mov_b32_e32 v15, v0
	v_mov_b32_e32 v113, v112
	v_mov_b32_e32 v114, v112
	v_mov_b32_e32 v115, v112
	v_mov_b32_e32 v116, v112
	v_mov_b32_e32 v117, v112
	v_mov_b32_e32 v118, v112
	v_mov_b32_e32 v119, v112
	v_mov_b32_e32 v120, v112
	v_mov_b32_e32 v121, v112
	v_mov_b32_e32 v122, v112
	v_mov_b32_e32 v123, v112
	v_mov_b32_e32 v124, v112
	v_mov_b32_e32 v125, v112
	v_mov_b32_e32 v126, v112
	v_mov_b32_e32 v127, v112
	v_mov_b32_e32 v97, v96
	v_mov_b32_e32 v98, v96
	v_mov_b32_e32 v99, v96
	v_mov_b32_e32 v100, v96
	v_mov_b32_e32 v101, v96
	v_mov_b32_e32 v102, v96
	v_mov_b32_e32 v103, v96
	v_mov_b32_e32 v104, v96
	v_mov_b32_e32 v105, v96
	v_mov_b32_e32 v106, v96
	v_mov_b32_e32 v107, v96
	v_mov_b32_e32 v108, v96
	v_mov_b32_e32 v109, v96
	v_mov_b32_e32 v110, v96
	v_mov_b32_e32 v111, v96
	v_mov_b32_e32 v81, v80
	v_mov_b32_e32 v82, v80
	v_mov_b32_e32 v83, v80
	v_mov_b32_e32 v84, v80
	v_mov_b32_e32 v85, v80
	v_mov_b32_e32 v86, v80
	v_mov_b32_e32 v87, v80
	v_mov_b32_e32 v88, v80
	v_mov_b32_e32 v89, v80
	v_mov_b32_e32 v90, v80
	v_mov_b32_e32 v91, v80
	v_mov_b32_e32 v92, v80
	v_mov_b32_e32 v93, v80
	v_mov_b32_e32 v94, v80
	v_mov_b32_e32 v95, v80
	v_mov_b32_e32 v49, v48
	v_mov_b32_e32 v50, v48
	v_mov_b32_e32 v51, v48
	v_mov_b32_e32 v52, v48
	v_mov_b32_e32 v53, v48
	v_mov_b32_e32 v54, v48
	v_mov_b32_e32 v55, v48
	v_mov_b32_e32 v56, v48
	v_mov_b32_e32 v57, v48
	v_mov_b32_e32 v58, v48
	v_mov_b32_e32 v59, v48
	v_mov_b32_e32 v60, v48
	v_mov_b32_e32 v61, v48
	v_mov_b32_e32 v62, v48
	v_mov_b32_e32 v63, v48
	s_ashr_i32 s45, s17, 6
	v_add3_u32 v238, 0, v138, v139
	v_lshl_add_u32 v239, v235, 2, s40
	v_lshlrev_b32_e32 v248, 6, v137
	s_add_u32 s46, s15, 0x1a0000
	v_lshl_add_u64 v[220:221], s[10:11], 0, v[208:209]
	s_sub_i32 s47, 0, s16
	v_mov_b32_e32 v226, 0xff800000
	v_mov_b32_e32 v251, 0
	s_mov_b64 s[14:15], 0
	v_mov_b32_e32 v208, 0
	v_mov_b32_e32 v227, 0xff800000
	s_add_i32 m0, s44, 0x4000
	s_nop 0
	global_load_lds_dwordx4 v[210:211], off
	s_add_i32 m0, s44, 0x4400
	s_nop 0
	global_load_lds_dwordx4 v[216:217], off
	s_waitcnt vmcnt(0) lgkmcnt(0)
	s_barrier
	v_add_u32_e32 v240, v236, v240
	v_add_u32_e32 v241, v236, v241
	v_add_u32_e32 v242, v236, v242
	v_add_u32_e32 v243, v236, v243
	v_add_u32_e32 v244, v236, v244
	v_add_u32_e32 v245, v236, v245
	v_add_u32_e32 v246, v236, v246
	v_add_u32_e32 v247, v236, v247
	v_sub_u32_e32 v237, v237, v236
	s_mov_b32 s48, 0
	v_mov_b32_e32 v228, s64
	ds_read_b32 v229, v228
	v_add3_u32 v254, v237, v240, s48
	ds_read_b128 v[128:131], v254
	ds_read_b128 v[132:135], v254 offset:8192
	ds_read_b128 v[136:139], v240
	v_add3_u32 v254, v237, v241, s48
	ds_read_b128 v[140:143], v254
	ds_read_b128 v[144:147], v254 offset:8192
	ds_read_b128 v[148:151], v241
	v_add3_u32 v254, v237, v242, s48
	ds_read_b128 v[152:155], v254
	ds_read_b128 v[156:159], v254 offset:8192
	ds_read_b128 v[192:195], v242
	v_add3_u32 v254, v237, v243, s48
	ds_read_b128 v[196:199], v254
	ds_read_b128 v[200:203], v254 offset:8192
	ds_read_b128 v[204:207], v243
	s_waitcnt lgkmcnt(9)
	v_mfma_f32_32x32x16_bf16 v[160:175], v[128:131], v[136:139], 0
	v_mfma_f32_32x32x16_bf16 v[176:191], v[132:135], v[136:139], 0
	s_waitcnt lgkmcnt(6)
	v_mfma_f32_32x32x16_bf16 v[160:175], v[140:143], v[148:151], v[160:175]
	v_mfma_f32_32x32x16_bf16 v[176:191], v[144:147], v[148:151], v[176:191]
	s_waitcnt lgkmcnt(3)
	v_mfma_f32_32x32x16_bf16 v[160:175], v[152:155], v[192:195], v[160:175]
	v_mfma_f32_32x32x16_bf16 v[176:191], v[156:159], v[192:195], v[176:191]
	s_waitcnt lgkmcnt(0)
	v_mfma_f32_32x32x16_bf16 v[160:175], v[196:199], v[204:207], v[160:175]
	v_mfma_f32_32x32x16_bf16 v[176:191], v[200:203], v[204:207], v[176:191]
	v_readfirstlane_b32 s50, v229
